# scheduling: attention unit order rotated per XCD so the weight-conversion bursts between units are spread over time
# baseline (speedup 1.0000x reference)
.LBB0_976:
	v_mbcnt_lo_u32_b32 v4, -1, 0
	v_mbcnt_hi_u32_b32 v4, -1, v4
	v_lshlrev_b32_e32 v4, 2, v4
	global_load_dword v2, v4, s[12:13]
	global_load_dword v0, v4, s[14:15]
	s_waitcnt vmcnt(0)
	v_and_b32_e32 v2, 0x7fffffff, v2
	v_and_b32_e32 v0, 0x7fffffff, v0
	s_nop 1
	v_max_f32_dpp v2, v2, v2 quad_perm:[1,0,3,2] row_mask:0xf bank_mask:0xf
	v_max_f32_dpp v0, v0, v0 quad_perm:[1,0,3,2] row_mask:0xf bank_mask:0xf
	s_nop 1
	v_max_f32_dpp v2, v2, v2 quad_perm:[2,3,0,1] row_mask:0xf bank_mask:0xf
	v_max_f32_dpp v0, v0, v0 quad_perm:[2,3,0,1] row_mask:0xf bank_mask:0xf
	s_nop 1
	v_max_f32_dpp v2, v2, v2 row_half_mirror row_mask:0xf bank_mask:0xf
	v_max_f32_dpp v0, v0, v0 row_half_mirror row_mask:0xf bank_mask:0xf
	s_nop 1
	v_max_f32_dpp v2, v2, v2 row_mirror row_mask:0xf bank_mask:0xf
	v_max_f32_dpp v0, v0, v0 row_mirror row_mask:0xf bank_mask:0xf
	s_nop 1
	v_readlane_b32 s16, v2, 0
	v_readlane_b32 s17, v2, 16
	s_nop 3
	s_max_u32 s16, s16, s17
	v_readlane_b32 s17, v2, 32
	s_nop 3
	s_max_u32 s16, s16, s17
	v_readlane_b32 s17, v2, 48
	s_nop 3
	s_max_u32 s16, s16, s17
	v_readlane_b32 s17, v0, 0
	v_mov_b32_e32 v2, s16
	v_readlane_b32 s16, v0, 16
	s_nop 3
	s_max_u32 s16, s16, s17
	v_readlane_b32 s17, v0, 32
	s_nop 3
	s_max_u32 s16, s16, s17
	v_readlane_b32 s17, v0, 48
	s_nop 3
	s_max_u32 s16, s16, s17
	s_nop 1
	v_mov_b32_e32 v0, s16
	s_cmp_ge_i32 s87, s53
	s_cbranch_scc1 .LBB0_1155
	s_add_u32 s66, s6, 0x27800000
	s_addc_u32 s67, s7, 0
	s_add_u32 s96, s8, 0x30000000
	v_readlane_b32 s6, v254, 42
	s_addc_u32 s97, s9, 0
	s_add_i32 s8, s6, s43
	s_and_b64 s[6:7], s[54:55], exec
	s_cselect_b32 s75, s8, 0
	s_cmp_gt_i32 s75, s43
	s_mul_hi_i32 s6, s43, 0x2aaaaaab
	s_cselect_b64 s[14:15], -1, 0
	s_lshr_b32 s7, s6, 31
	s_ashr_i32 s6, s6, 9
	s_add_i32 s6, s6, s7
	s_mul_i32 s7, s6, 0xfffff400
	s_add_i32 s8, s7, s43
	s_cmpk_gt_i32 s8, 0x7ff
	s_cselect_b64 s[16:17], -1, 0
	s_add_i32 s7, s8, 0xfffff800
	s_lshl_b32 s9, s6, 5
	s_lshr_b32 s6, s7, 5
	s_add_i32 s6, s6, s9
	s_ashr_i32 s7, s6, 31
	s_lshl_b64 s[18:19], s[6:7], 20
	s_ashr_i32 s6, s8, 6
	v_mul_f32_e32 v2, 0x4138aa3b, v2
	s_add_i32 s6, s6, s9
	v_mul_f32_e32 v0, v0, v2
	s_ashr_i32 s7, s6, 31
	v_mul_f32_e32 v210, 0x3f828f5c, v0
	s_lshl_b32 s68, s43, 8
	s_lshl_b32 s54, s43, 4
	s_lshl_b64 s[20:21], s[6:7], 23
	s_lshl_b64 s[22:23], s[6:7], 21
	s_mov_b32 s6, 0x42700000
	s_mov_b32 s74, 0
	s_lshl_b32 s48, s43, 5
	s_and_b32 s52, s68, 0x300
	s_and_b32 s46, s68, 0x700
	v_cmp_ge_f32_e64 s[6:7], s6, v210
	s_lshr_b32 s8, s87, 5
	s_add_i32 s9, s8, -6
	s_cmp_gt_u32 s8, 5
	s_cselect_b32 s8, s9, s8
	s_lshl_b32 s8, s8, 8
	s_add_i32 s83, s87, s8
	s_add_i32 s87, s43, 2
	s_add_i32 s51, s54, 32
	s_addk_i32 s68, 0x200
	s_branch .LBB0_980
.LBB0_979:
	s_or_b64 exec, exec, s[8:9]
	s_mul_i32 s9, s58, 0x880000
	s_waitcnt lgkmcnt(0)
	s_mul_hi_i32 s8, s58, 0x880000
	s_add_u32 s10, s96, s9
	ds_read_b128 v[2:5], v238 offset:49280
	ds_read_b128 v[6:9], v238 offset:49312
	s_addc_u32 s11, s97, s8
	s_and_b64 s[8:9], exec, s[24:25]
	s_movk_i32 s8, 0x500
	s_cselect_b32 s8, 0x200, s8
	s_add_u32 s8, s10, s8
	s_waitcnt lgkmcnt(1)
	v_rcp_f32_e32 v0, v2
	s_addc_u32 s9, s11, 0
	s_add_u32 s10, s8, s26
	v_rcp_f32_e32 v10, v3
	s_addc_u32 s11, s9, s27
	s_lshl_b32 s12, s89, 12
	s_add_i32 s12, s12, 0
	v_lshlrev_b32_e32 v49, 1, v231
	v_lshlrev_b32_e32 v50, 9, v232
	v_mul_f32_e32 v32, v32, v0
	v_mul_f32_e32 v0, v16, v0
	v_add3_u32 v49, s12, v49, v50
	v_cvt_pk_bf16_f32 v0, v0, s0
	v_rcp_f32_e32 v11, v4
	v_rcp_f32_e32 v12, v5
	s_waitcnt lgkmcnt(0)
	v_rcp_f32_e32 v13, v6
	ds_read_b128 v[2:5], v238 offset:49344
	v_rcp_f32_e32 v14, v7
	v_rcp_f32_e32 v15, v8
	v_rcp_f32_e32 v48, v9
	ds_read_b128 v[6:9], v238 offset:49376
	ds_write_b16 v49, v0 offset:51264
	v_mul_f32_e32 v0, v33, v10
	v_cvt_pk_bf16_f32 v0, v0, s0
	ds_write_b16 v49, v0 offset:51328
	v_mul_f32_e32 v0, v17, v10
	v_cvt_pk_bf16_f32 v0, v0, s0
	ds_write_b16 v49, v0 offset:51392
	v_mul_f32_e32 v0, v34, v11
	v_cvt_pk_bf16_f32 v0, v0, s0
	ds_write_b16 v49, v0 offset:51456
	v_mul_f32_e32 v0, v18, v11
	v_cvt_pk_bf16_f32 v0, v0, s0
	ds_write_b16 v49, v0 offset:51520
	v_mul_f32_e32 v0, v35, v12
	v_cvt_pk_bf16_f32 v0, v0, s0
	ds_write_b16 v49, v0 offset:51584
	v_mul_f32_e32 v0, v19, v12
	v_cvt_pk_bf16_f32 v0, v0, s0
	ds_write_b16 v49, v0 offset:51648
	v_mul_f32_e32 v0, v36, v13
	v_cvt_pk_bf16_f32 v0, v0, s0
	ds_write_b16 v49, v0 offset:52224
	v_mul_f32_e32 v0, v20, v13
	v_cvt_pk_bf16_f32 v0, v0, s0
	ds_write_b16 v49, v0 offset:52288
	v_mul_f32_e32 v0, v37, v14
	v_cvt_pk_bf16_f32 v0, v0, s0
	ds_write_b16 v49, v0 offset:52352
	v_mul_f32_e32 v0, v21, v14
	v_cvt_pk_bf16_f32 v0, v0, s0
	ds_write_b16 v49, v0 offset:52416
	v_mul_f32_e32 v0, v38, v15
	v_cvt_pk_bf16_f32 v0, v0, s0
	ds_write_b16 v49, v0 offset:52480
	v_mul_f32_e32 v0, v22, v15
	v_cvt_pk_bf16_f32 v0, v0, s0
	s_waitcnt lgkmcnt(13)
	v_rcp_f32_e32 v2, v2
	ds_write_b16 v49, v0 offset:52544
	v_mul_f32_e32 v0, v39, v48
	v_cvt_pk_bf16_f32 v0, v0, s0
	ds_write_b16 v49, v0 offset:52608
	v_mul_f32_e32 v0, v23, v48
	v_cvt_pk_bf16_f32 v0, v0, s0
	v_rcp_f32_e32 v3, v3
	ds_write_b16 v49, v0 offset:52672
	v_mul_f32_e32 v0, v40, v2
	v_cvt_pk_bf16_f32 v0, v0, s0
	ds_write_b16 v49, v0 offset:53248
	v_mul_f32_e32 v0, v24, v2
	v_cvt_pk_bf16_f32 v0, v0, s0
	v_rcp_f32_e32 v4, v4
	ds_write_b16 v49, v0 offset:53312
	v_mul_f32_e32 v0, v41, v3
	v_cvt_pk_bf16_f32 v0, v0, s0
	ds_write_b16 v49, v0 offset:53376
	v_mul_f32_e32 v0, v25, v3
	v_cvt_pk_bf16_f32 v0, v0, s0
	v_rcp_f32_e32 v5, v5
	ds_write_b16 v49, v0 offset:53440
	v_mul_f32_e32 v0, v42, v4
	v_cvt_pk_bf16_f32 v0, v0, s0
	ds_write_b16 v49, v0 offset:53504
	v_mul_f32_e32 v0, v26, v4
	v_cvt_pk_bf16_f32 v0, v0, s0
	s_waitcnt lgkmcnt(14)
	v_rcp_f32_e32 v6, v6
	ds_write_b16 v49, v0 offset:53568
	v_mul_f32_e32 v0, v43, v5
	v_cvt_pk_bf16_f32 v0, v0, s0
	ds_write_b16 v49, v0 offset:53632
	v_mul_f32_e32 v0, v27, v5
	v_cvt_pk_bf16_f32 v0, v0, s0
	v_rcp_f32_e32 v7, v7
	ds_write_b16 v49, v0 offset:53696
	v_mul_f32_e32 v0, v44, v6
	v_cvt_pk_bf16_f32 v0, v0, s0
	ds_write_b16 v49, v0 offset:54272
	v_mul_f32_e32 v0, v28, v6
	v_cvt_pk_bf16_f32 v0, v0, s0
	v_rcp_f32_e32 v8, v8
	ds_write_b16 v49, v0 offset:54336
	v_mul_f32_e32 v0, v45, v7
	v_cvt_pk_bf16_f32 v0, v0, s0
	ds_write_b16 v49, v0 offset:54400
	v_mul_f32_e32 v0, v29, v7
	v_cvt_pk_bf16_f32 v0, v0, s0
	v_rcp_f32_e32 v9, v9
	ds_write_b16 v49, v0 offset:54464
	v_mul_f32_e32 v0, v46, v8
	v_cvt_pk_bf16_f32 v0, v0, s0
	ds_write_b16 v49, v0 offset:54528
	v_mul_f32_e32 v0, v30, v8
	v_cvt_pk_bf16_f32 v0, v0, s0
	ds_write_b16 v49, v0 offset:54592
	v_mul_f32_e32 v0, v47, v9
	v_cvt_pk_bf16_f32 v0, v0, s0
	ds_write_b16 v49, v0 offset:54656
	v_mul_f32_e32 v0, v31, v9
	v_cvt_pk_bf16_f32 v0, v0, s0
	s_lshl_b64 s[8:9], s[28:29], 11
	ds_write_b16 v49, v0 offset:54720
	v_lshlrev_b32_e32 v0, 1, v230
	v_cvt_pk_bf16_f32 v32, v32, s0
	s_add_u32 s8, s10, s8
	v_and_b32_e32 v0, 0x70, v0
	ds_write_b16 v49, v32 offset:51200
	s_addc_u32 s9, s11, s9
	v_lshrrev_b32_e32 v14, 3, v211
	v_add_u32_e32 v15, s12, v0
	s_waitcnt lgkmcnt(0)
	v_lshl_add_u64 v[10:11], s[8:9], 0, v[0:1]
	v_lshl_add_u32 v0, v14, 7, v15
	v_or_b32_e32 v16, 8, v14
	ds_read_b128 v[2:5], v0 offset:51200
	v_lshl_add_u32 v6, v16, 7, v15
	ds_read_b128 v[6:9], v6 offset:51200
	v_lshlrev_b32_e32 v0, 11, v14
	v_lshl_add_u64 v[12:13], v[10:11], 0, v[0:1]
	v_lshlrev_b32_e32 v0, 11, v16
	s_waitcnt lgkmcnt(1)
	global_store_dwordx4 v[12:13], v[2:5], off
	s_add_i32 s74, s74, 1
	v_lshl_add_u64 v[2:3], v[10:11], 0, v[0:1]
	v_or_b32_e32 v0, 16, v14
	s_waitcnt lgkmcnt(0)
	global_store_dwordx4 v[2:3], v[6:9], off
	v_lshl_add_u32 v2, v0, 7, v15
	v_or_b32_e32 v14, 24, v14
	ds_read_b128 v[2:5], v2 offset:51200
	v_lshl_add_u32 v6, v14, 7, v15
	ds_read_b128 v[6:9], v6 offset:51200
	v_lshlrev_b32_e32 v0, 11, v0
	v_lshl_add_u64 v[12:13], v[10:11], 0, v[0:1]
	v_lshlrev_b32_e32 v0, 11, v14
	s_waitcnt lgkmcnt(1)
	global_store_dwordx4 v[12:13], v[2:5], off
	v_readlane_b32 s8, v255, 45
	s_lshr_b32 s9, s8, 5
	s_add_i32 vcc_lo, s9, -6
	s_cmp_gt_u32 s9, 5
	s_cselect_b32 s9, vcc_lo, s9
	s_add_i32 s9, s9, s74
	s_add_i32 vcc_lo, s9, -6
	s_cmp_gt_u32 s9, 5
	s_cselect_b32 s9, vcc_lo, s9
	s_cmp_gt_u32 s74, 5
	s_cselect_b32 s9, s74, s9
	s_lshl_b32 s9, s9, 8
	s_add_i32 s83, s8, s9
	s_cmp_lt_i32 s83, s53
	s_nop 0
	v_lshl_add_u64 v[2:3], v[10:11], 0, v[0:1]
	s_waitcnt lgkmcnt(0)
	global_store_dwordx4 v[2:3], v[6:9], off
	s_waitcnt lgkmcnt(0)
	s_barrier
	s_cbranch_scc0 .LBB0_1154
